# balanced two-sided drain: before-attention converters stop at the midpoint of the remaining queue range, fixed quota lifted
# baseline (speedup 1.0000x reference)
; #define LAS __attribute__((address_space(3)))
; __device__ __forceinline__ unsigned xb_ld(unsigned* p)              { return __hip_atomic_load(p, __ATOMIC_RELAXED, __HIP_MEMORY_SCOPE_AGENT); }
; __device__ __forceinline__ unsigned xb_add(unsigned* p, unsigned v) { return __hip_atomic_fetch_add(p, v, __ATOMIC_RELAXED, __HIP_MEMORY_SCOPE_AGENT); }
;     __device__ __forceinline__ unsigned char* ws() const { return *(unsigned char* const __attribute__((address_space(4)))*)(p + 232); }
;     volatile LAS unsigned* st = (volatile LAS unsigned*)(lds + MISC_OFF) + 8;
;     unsigned* qw = (unsigned*)(ws + WS_CTL) + CW_Q;
;     int tl = tid_x(); asm volatile("" : "+v"(tl));
;     const int wave = __builtin_amdgcn_readfirstlane(tl >> 6), lane = tl & 63;
;     LAS float* scr = (LAS float*)(lds + wave * 16640);
;     __syncthreads();
;     unsigned ahead = 0xFFFFFFFFu;
;     if (tl == 0 && max_claims > 0) { if (xb_ld(qw) < (unsigned)target) ahead = xb_add(qw, 32u); }
.LBB0_690:
	v_readlane_b32 s0, v254, 2
	v_readlane_b32 s1, v254, 3
	s_and_b64 vcc, exec, s[0:1]
	s_mov_b64 s[36:37], 0x100
	s_waitcnt lgkmcnt(0)
	s_barrier
	s_cbranch_vccz .LBB0_782
	v_readlane_b32 s0, v254, 60
	s_mul_i32 s27, s0, 0xc300
	s_add_i32 s25, s27, 0xc300
	s_add_u32 s4, s8, 0x20000
	s_getreg_b32 s0, hwreg(HW_REG_HW_ID, 0, 6)
	s_addc_u32 s5, s9, 0
	s_and_b32 s0, s0, 63
	s_lshl_b32 s0, s0, 2
	s_add_i32 s0, s0, 0
	s_add_i32 s0, s0, 0x23f00
	v_mov_b32_e32 v0, s0
	ds_read_b32 v0, v0
	v_mbcnt_lo_u32_b32 v1, -1, 0
	v_mbcnt_hi_u32_b32 v1, -1, v1
	v_readlane_b32 s1, v254, 61
	v_mov_b32_e32 v129, -1
	s_waitcnt lgkmcnt(0)
	v_readfirstlane_b32 s0, v0
	s_nop 1
	v_lshl_add_u32 v0, s0, 6, v1
	s_nop 0
	v_readfirstlane_b32 s14, v0
	v_cmp_eq_u32_e64 s[2:3], 0, v0
	s_barrier
	s_and_saveexec_b64 s[0:1], s[2:3]
	s_cbranch_execz .LBB0_696
	global_load_dword v1, v193, s[4:5] sc1
	v_mov_b32_e32 v129, -1
	s_waitcnt vmcnt(0)
	v_readfirstlane_b32 s100, v1
	s_add_u32 s100, s100, s25
	s_lshr_b32 s100, s100, 1
	s_add_u32 s100, s100, 31
	s_and_b32 s100, s100, -32
	s_sub_u32 s101, s100, 32
	v_cmp_le_u32_e32 vcc, s25, v1
	s_cbranch_vccnz .LBB0_696
	s_mov_b64 s[12:13], exec
	v_mbcnt_lo_u32_b32 v1, s12, 0
	v_mbcnt_hi_u32_b32 v1, s13, v1
	v_cmp_eq_u32_e32 vcc, 0, v1
	s_and_saveexec_b64 s[10:11], vcc
	s_cbranch_execz .LBB0_695
	s_bcnt1_i32_b64 s12, s[12:13]
	s_lshl_b32 s12, s12, 5
	v_mov_b32_e32 v2, s12
	global_atomic_add v2, v193, v2, s[4:5] sc0

; __device__ __forceinline__ unsigned xb_add(unsigned* p, unsigned v) { return __hip_atomic_fetch_add(p, v, __ATOMIC_RELAXED, __HIP_MEMORY_SCOPE_AGENT); }
;     ...
;     for (int nc = 0; nc < max_claims; ++nc) {
;         if (tl == 0) { st[6] = ahead; if (ahead < (unsigned)target && nc + 1 < max_claims) ahead = (ahead + 32u < (unsigned)target) ? xb_add(qw, 32u) : 0xFFFFFFFFu; }
;         __syncthreads();
.LBB0_698:
	s_and_saveexec_b64 s[0:1], s[2:3]
	s_cbranch_execz .LBB0_706
	v_readlane_b32 s14, v254, 27
	s_cmp_lt_u32 s30, 30
	v_cmp_gt_u32_e32 vcc, s101, v129
	v_mov_b32_e32 v139, s14
	s_cselect_b64 s[14:15], -1, 0
	s_and_b64 s[16:17], vcc, s[14:15]
	ds_write_b32 v139, v129
	s_nop 1
	v_mov_b32_e32 v129, -1
	s_and_saveexec_b64 s[14:15], s[16:17]
	s_cbranch_execz .LBB0_705
	s_mov_b64 vcc, exec
	v_mov_b32_e32 v129, -1
	s_and_saveexec_b64 s[16:17], vcc
	s_cbranch_execz .LBB0_704
	s_mov_b64 s[20:21], exec
	v_mbcnt_lo_u32_b32 v129, s20, 0
	v_mbcnt_hi_u32_b32 v129, s21, v129
	v_cmp_eq_u32_e32 vcc, 0, v129
	s_and_saveexec_b64 s[18:19], vcc
	s_cbranch_execz .LBB0_703
	s_bcnt1_i32_b64 s20, s[20:21]
	s_lshl_b32 s20, s20, 5
	v_mov_b32_e32 v139, s20
	global_atomic_add v139, v193, v139, s[4:5] sc0

; __device__ __forceinline__ unsigned xb_add(unsigned* p, unsigned v) { return __hip_atomic_fetch_add(p, v, __ATOMIC_RELAXED, __HIP_MEMORY_SCOPE_AGENT); }
;     __device__ __forceinline__ unsigned char* ws() const { return *(unsigned char* const __attribute__((address_space(4)))*)(p + 232); }
;     ...
;     for (int nc = 0; nc < max_claims; ++nc) {
;         if (tl == 0) { st[6] = ahead; if (ahead < (unsigned)target && nc + 1 < max_claims) ahead = (ahead + 32u < (unsigned)target) ? xb_add(qw, 32u) : 0xFFFFFFFFu; }
;         __syncthreads();
;         const unsigned base = st[6];
;         if (base < (unsigned)Q_TOTAL) {
;             const int q0 = (int)base + wave; const bool v0 = q0 < Q_TOTAL, v1 = q0 + 8 < Q_TOTAL, v2 = q0 + 16 < Q_TOTAL, v3 = q0 + 24 < Q_TOTAL;
;             float ta[64], tb[64]; CvtDesc da, db;
;             if (v0) { da = conv_expert_desc(a, ws, q0); cvt_load(da, ta, lane); }
;             if (v1) { db = conv_expert_desc(a, ws, q0 + 8); cvt_load(db, tb, lane); }
;             if (v0) cvt_finish(da, ta, scr, lane);
;             if (v2) { da = conv_expert_desc(a, ws, q0 + 16); cvt_load(da, ta, lane); }
;             if (v1) cvt_finish(db, tb, scr, lane);
;             if (v3) { db = conv_expert_desc(a, ws, q0 + 24); cvt_load(db, tb, lane); }
;             if (v2) cvt_finish(da, ta, scr, lane);
;             if (v3) cvt_finish(db, tb, scr, lane);
;         }
;         if (base >= (unsigned)target) break;
;         __syncthreads();
.LBB0_779:
	s_cmp_ge_u32 s35, s25
	s_mov_b64 s[0:1], -1
	s_cbranch_scc1 .LBB0_697
	s_add_i32 s30, s30, 1
	s_cmp_eq_u32 s30, 31
	s_cselect_b64 s[0:1], -1, 0
	s_barrier
	s_branch .LBB0_697

; __device__ __forceinline__ unsigned xb_add(unsigned* p, unsigned v) { return __hip_atomic_fetch_add(p, v, __ATOMIC_RELAXED, __HIP_MEMORY_SCOPE_AGENT); }
;     ...
;     for (int nc = 0; nc < max_claims; ++nc) {
;         if (tl == 0) { st[6] = ahead; if (ahead < (unsigned)target && nc + 1 < max_claims) ahead = (ahead + 32u < (unsigned)target) ? xb_add(qw, 32u) : 0xFFFFFFFFu; }
;         __syncthreads();
.LBB0_803:
	s_and_saveexec_b64 s[0:1], s[2:3]
	s_cbranch_execz .LBB0_811
	v_readlane_b32 s14, v254, 27
	s_cmp_lt_u32 s30, 30
	v_cmp_gt_u32_e32 vcc, s25, v129
	v_mov_b32_e32 v139, s14
	s_cselect_b64 s[14:15], -1, 0
	s_and_b64 s[16:17], vcc, s[14:15]
	ds_write_b32 v139, v129
	s_and_saveexec_b64 s[14:15], s[16:17]
	s_cbranch_execz .LBB0_810
	v_cmp_gt_u32_e32 vcc, s27, v129
	v_mov_b32_e32 v129, -1
	s_and_saveexec_b64 s[16:17], vcc
	s_cbranch_execz .LBB0_809
	s_mov_b64 s[20:21], exec
	v_mbcnt_lo_u32_b32 v129, s20, 0
	v_mbcnt_hi_u32_b32 v129, s21, v129
	v_cmp_eq_u32_e32 vcc, 0, v129
	s_and_saveexec_b64 s[18:19], vcc
	s_cbranch_execz .LBB0_808
	s_bcnt1_i32_b64 s20, s[20:21]
	s_lshl_b32 s20, s20, 5
	v_mov_b32_e32 v139, s20
	global_atomic_add v139, v193, v139, s[4:5] sc0
